# global-attention tile prologue: the two 6-hop ds_bpermute max reductions replaced by DPP + permlane swaps
# baseline (speedup 1.0000x reference)
; template <int KIND_CT  >
; __device__ __forceinline__ void attn_tile(const Ctx& c, int layer, int idx, unsigned char* lds) {
;     ...
;     if (kind == 0) {
;         float gm = fmaxf(fabsf(c.in(20)[layer * 64 + lane]), 0.f), km = fabsf(c.in(21)[layer * 64 + lane]);
; #pragma unroll
;         for (int o = 1; o < 64; o <<= 1) { gm = fmaxf(gm, __shfl_xor(gm, o)); km = fmaxf(km, __shfl_xor(km, o)); }
;         fixedref = __builtin_amdgcn_readfirstlane((int)(gm * km * 8.f * 1.4426950408889634f < 40.f)) != 0;
;         if (fixedref) m = 0.f;
.LBB0_404:
	s_load_dwordx4 s[48:51], s[0:1], 0xa0
	v_readlane_b32 s6, v251, 15
	v_cmp_lt_i32_e32 vcc, v229, v228
	s_nop 0
	v_or_b32_e32 v6, s6, v119
	v_ashrrev_i32_e32 v7, 31, v6
	v_lshlrev_b64 v[6:7], 2, v[6:7]
	s_waitcnt lgkmcnt(0)
	v_lshl_add_u64 v[8:9], s[48:49], 0, v[6:7]
	v_lshl_add_u64 v[6:7], s[50:51], 0, v[6:7]
	global_load_dword v2, v[8:9], off
	global_load_dword v5, v[6:7], off
	s_mov_b32 s6, 0x42200000
	s_waitcnt vmcnt(0)
	v_max_f32_e64 v2, |v2|, |v2|
	v_max_f32_e64 v5, |v5|, |v5|
	v_max_f32_e32 v2, 0, v2
	s_nop 1
	v_max_f32_dpp v2, v2, v2 quad_perm:[1,0,3,2] row_mask:0xf bank_mask:0xf
	v_max_f32_dpp v5, v5, v5 quad_perm:[1,0,3,2] row_mask:0xf bank_mask:0xf
	s_nop 0
	v_max_f32_dpp v2, v2, v2 quad_perm:[2,3,0,1] row_mask:0xf bank_mask:0xf
	v_max_f32_dpp v5, v5, v5 quad_perm:[2,3,0,1] row_mask:0xf bank_mask:0xf
	s_nop 0
	v_max_f32_dpp v2, v2, v2 row_half_mirror row_mask:0xf bank_mask:0xf
	v_max_f32_dpp v5, v5, v5 row_half_mirror row_mask:0xf bank_mask:0xf
	s_nop 0
	v_max_f32_dpp v2, v2, v2 row_mirror row_mask:0xf bank_mask:0xf
	v_max_f32_dpp v5, v5, v5 row_mirror row_mask:0xf bank_mask:0xf
	s_nop 0
	v_mov_b32_e32 v6, v2
	v_mov_b32_e32 v7, v5
	s_nop 1
	v_permlane16_swap_b32_e32 v2, v6
	v_permlane16_swap_b32_e32 v5, v7
	v_max_f32_e32 v2, v2, v6
	v_max_f32_e32 v5, v5, v7
	v_mov_b32_e32 v6, v2
	v_mov_b32_e32 v7, v5
	s_nop 1
	v_permlane32_swap_b32_e32 v2, v6
	v_permlane32_swap_b32_e32 v5, v7
	v_max_f32_e32 v2, v2, v6
	v_max_f32_e32 v5, v5, v7
	v_mul_f32_e32 v2, v2, v5
	v_mul_f32_e32 v2, 0x41000000, v2
	v_mul_f32_e32 v2, 0x3fb8aa3b, v2
	v_cmp_gt_f32_e32 vcc, s6, v2
	s_nop 1
	v_cndmask_b32_e64 v2, 0, 1, vcc
	s_nop 0
	v_readfirstlane_b32 s6, v2
	s_bitcmp1_b32 s6, 0
	s_cselect_b64 s[28:29], -1, 0
	v_cndmask_b32_e64 v132, v132, 0, s[28:29]
